# op phase: upper half of the grid starts ~10us later (epilogue HBM traffic of one half under the other half's K-loop)
# speedup vs baseline: 1.0167x; 1.0139x over previous
; #define LAS __attribute__((address_space(3)))
; #define PG8_BAR __builtin_amdgcn_s_barrier()
;     const int tid = opaque_tid(), wid = __builtin_amdgcn_readfirstlane(tid >> 6), lane = tid & 63, wr = wid >> 2, wc = wid & 3, fr = lane & 15, fq = lane >> 4;
;     const int nt = K / BK;
;     const unsigned ldaA = lda_in ? lda_in : (unsigned)(K * 2);
;     unsigned voffA[2], voffB[2];
; #pragma unroll
;     for (int i = 0; i < 2; ++i) { int R, C; stage_rc(tid * 16 + i * 8192, R, C); const int Rb = Epi::PERM ? ((R & ~31) + perm32(R & 31)) : R;
;         voffA[i] = (unsigned)R * ldaA + (unsigned)C * 2u; voffB[i] = (unsigned)(Rb * K + C) * 2u; }
;     const size_t kstep = (size_t)(BK * 2);
;     const size_t hstep = (size_t)HALF * K * 2;
;     const size_t kstepA = kstepA_in ? kstepA_in : kstep, hstepA = (size_t)HALF * ldaA;
;     const unsigned ldsw = (unsigned)wid * 1024u;
;     const int aoff = lds_byte(wr * 64 + fr, fq * 8), boff = lds_byte(wc * 32 + fr, fq * 8);
;     ...
;     Unit cur, nxt; int ui = 0;
;     if (!S.next(0, cur)) return;
;     f32x4 acc[2][2][4][2];
; #pragma unroll
;     for (int a = 0; a < 2; ++a)
; #pragma unroll
;         for (int b = 0; b < 2; ++b)
; #pragma unroll
;             for (int m = 0; m < 4; ++m)
; #pragma unroll
;                 for (int n = 0; n < 2; ++n) acc[a][b][m][n] = (f32x4){0.f, 0.f, 0.f, 0.f};
;     bf16x8 At[4][2], B0[2][2], B1[2][2];
;     const char* cA = cur.a; const char* cB = cur.b;
;     PG8_STAGE(PG8_SB(0, 0), cB, voffB); PG8_STAGE(PG8_SB(0, 1), cB + hstep, voffB); PG8_STAGE(PG8_SA(0, 0), cA, voffA); PG8_STAGE(PG8_SA(0, 1), cA + hstepA, voffA);
;     if (wr == 1) PG8_BAR;
;     PG8_WAIT_V(2); PG8_BAR;
;     PG8_STAGE(PG8_SB(1, 0), cB + kstep, voffB); PG8_STAGE(PG8_SA(1, 0), cA + kstepA, voffA); PG8_STAGE(PG8_SB(1, 1), cB + hstep + kstep, voffB);
;     PG8_WAIT_V(6); PG8_BAR;
; __device__ __forceinline__ void op_mfma(const Args& a, LAS unsigned char* lds, int layer, bf16_t* outp = nullptr) {
;     pg8::DenseOrder So; So.init(a.ws + WS_ACT, a.ws + WS_WOUT + (size_t)layer * D * D * 2, NTOK, D, D, gridDim.x, blockIdx.x, (size_t)256 * 128);
;     bf16_t* xb = (bf16_t*)(a.ws + WS_XB);
;     EpiOut E{layer == 0 ? a.in[I_X] : nullptr, xb, outp ? outp : xb, (const float*)(a.ws + WS_MOD) + (size_t)layer * NB * 6144 + 2048};
;     pg8::gemm_phase<EpiOut, pg8::DenseOrder>(lds, D, So, E, 128u, (size_t)NTOK * 128);
.LBB0_704:
	s_or_b64 exec, exec, s[38:39]
	s_cmp_lt_u32 s61, 128
	s_cbranch_scc1 .Lstag_op_done
	s_lshr_b32 vcc_lo, s61, 2
	s_and_b32 vcc_lo, vcc_lo, 0
	s_add_u32 vcc_lo, vcc_lo, 1
	s_mul_i32 vcc_lo, vcc_lo, 3
.Lstag_op_loop:
	s_sleep 110
	s_sub_u32 vcc_lo, vcc_lo, 1
	s_cmp_lg_u32 vcc_lo, 0
	s_cbranch_scc1 .Lstag_op_loop
.Lstag_op_done:
	v_readlane_b32 s4, v255, 11
	v_mov_b32_e32 v12, v0
	v_readlane_b32 s5, v255, 12
	s_waitcnt lgkmcnt(0)
	s_barrier
	s_andn2_b64 vcc, exec, s[4:5]
	v_readfirstlane_b32 s4, v12
	s_cbranch_vccnz .LBB0_728
	v_lshlrev_b32_e32 v1, 4, v12
	v_add_u32_e32 v2, 0x2000, v1
	v_ashrrev_i32_e32 v3, 31, v2
	v_lshrrev_b32_e32 v3, 22, v3
	v_add_u32_e32 v3, v2, v3
	v_ashrrev_i32_e32 v6, 10, v3
	v_mul_i32_i24_e32 v3, 0x400, v6
	v_sub_u32_e32 v2, v2, v3
	v_lshrrev_b32_e32 v3, 4, v2
	v_bitop3_b32 v2, v3, v2, 32 bitop3:0x6c
	v_ashrrev_i32_e32 v3, 31, v2
	v_lshrrev_b32_e32 v3, 26, v3
	v_add_u32_e32 v3, v2, v3
	v_lshlrev_b32_e32 v4, 3, v6
	v_ashrrev_i32_e32 v7, 6, v3
	v_and_b32_e32 v4, -16, v4
	s_lshl_b64 s[6:7], s[62:63], 21
	v_readlane_b32 s2, v253, 19
	v_add_u32_e32 v4, v7, v4
	s_add_u32 s2, s2, s6
	v_and_b32_e32 v5, 3, v7
	s_mov_b32 s6, 0x1fffe0
	v_lshrrev_b32_e32 v8, 2, v4
	v_lshlrev_b32_e32 v9, 1, v4
	v_and_b32_e32 v3, 0xc0, v3
	v_and_or_b32 v5, v4, s6, v5
	v_and_b32_e32 v8, 4, v8
	v_and_b32_e32 v9, 24, v9
	v_sub_u32_e32 v2, v2, v3
	v_or3_b32 v5, v5, v8, v9
	v_lshlrev_b32_e32 v8, 5, v6
	v_ashrrev_i16_sdwa v2, v238, sext(v2) dst_sel:DWORD dst_unused:UNUSED_PAD src0_sel:DWORD src1_sel:BYTE_0
	v_and_b32_e32 v9, 32, v8
	v_bfe_i32 v8, v2, 0, 16
	v_add_lshl_u32 v2, v9, v8, 1
	v_lshl_add_u32 v188, v5, 11, v2
	v_lshl_add_u32 v190, v4, 7, v2
	v_bfe_i32 v2, v12, 27, 1
	v_lshrrev_b32_e32 v2, 22, v2
	v_add_u32_e32 v2, v1, v2
	v_and_b32_e32 v2, 0xfffffc00, v2
	v_sub_u32_e32 v1, v1, v2
	v_lshrrev_b32_e32 v2, 4, v1
	v_bitop3_b32 v2, v2, v1, 32 bitop3:0x6c
	v_ashrrev_i32_e32 v1, 31, v1
	v_lshrrev_b32_e32 v1, 26, v1
	v_add_u32_e32 v1, v2, v1
	v_ashrrev_i32_e32 v9, 6, v1
	v_ashrrev_i32_e32 v1, 31, v12
	v_lshrrev_b32_e32 v1, 26, v1
	v_add_u32_e32 v1, v12, v1
	v_ashrrev_i32_e32 v10, 6, v1
	v_lshlrev_b32_e32 v1, 3, v10
	v_and_b32_e32 v1, -16, v1
	v_add_u32_e32 v1, v9, v1
	v_and_b32_e32 v3, 3, v9
	v_lshrrev_b32_e32 v4, 2, v1
	v_lshlrev_b32_e32 v5, 1, v1
	v_and_or_b32 v3, v1, s6, v3
	v_and_b32_e32 v4, 4, v4
	v_and_b32_e32 v5, 24, v5
	v_readlane_b32 s5, v253, 20
	v_or3_b32 v3, v3, v4, v5
	v_mul_i32_i24_e32 v5, 64, v9
	s_addc_u32 s30, s5, s7
	s_ashr_i32 s5, s4, 6
	v_sub_u32_e32 v2, v2, v5
	s_ashr_i32 s10, s4, 8
	s_lshl_b32 s31, s5, 10
	v_lshlrev_b32_e32 v4, 5, v10
	v_ashrrev_i16_sdwa v2, v238, sext(v2) dst_sel:DWORD dst_unused:UNUSED_PAD src0_sel:DWORD src1_sel:BYTE_0
	v_readlane_b32 s6, v253, 39
	v_and_b32_e32 v4, 32, v4
	v_bfe_i32 v11, v2, 0, 16
	v_readlane_b32 s7, v253, 40
	s_add_u32 s22, s2, s6
	v_add_lshl_u32 v2, v4, v11, 1
	s_addc_u32 s23, s30, s7
	s_add_i32 s34, s31, 0
	v_lshl_add_u32 v34, v3, 11, v2
	s_add_i32 m0, s34, 0x10000
	v_lshl_add_u32 v192, v1, 7, v2
	global_load_lds_dwordx4 v34, s[22:23]
	s_add_i32 m0, s34, 0x12000
	s_add_u32 s6, s22, 0x40000
	global_load_lds_dwordx4 v188, s[22:23]
	s_addc_u32 s7, s23, 0
	s_add_i32 m0, s34, 0x14000
	s_add_i32 s35, s34, 0x2000
	global_load_lds_dwordx4 v34, s[6:7]
	s_add_i32 m0, s34, 0x16000
	s_add_i32 s38, s34, 0x4000
	global_load_lds_dwordx4 v188, s[6:7]
	v_readlane_b32 s6, v253, 43
	s_mov_b32 m0, s34
	v_readlane_b32 s7, v253, 44
	s_add_i32 s39, s34, 0x6000
	v_mov_b32_e32 v189, v35
	s_cmp_eq_u32 s10, 1
	v_lshl_add_u64 v[2:3], s[22:23], 0, v[34:35]
	v_lshl_add_u64 v[4:5], s[22:23], 0, v[188:189]
	global_load_lds_dwordx4 v192, s[6:7]
	s_mov_b32 m0, s35
	s_nop 0
	global_load_lds_dwordx4 v190, s[6:7]
	v_readlane_b32 s6, v253, 41
	s_mov_b32 m0, s38
	v_readlane_b32 s7, v253, 42
	s_nop 4
	global_load_lds_dwordx4 v192, s[6:7]
	s_mov_b32 m0, s39
	s_nop 0
	global_load_lds_dwordx4 v190, s[6:7]
	s_cselect_b64 s[6:7], -1, 0
	s_cmp_lg_u32 s10, 1
	s_cbranch_scc1 .LBB0_707
	s_barrier
